# v57 plus dense down-projection visits its row tiles in the opposite half order (pm xor 8) so that the most recently written SwiGLU rows are read first
# speedup vs baseline: 1.0073x; 1.0065x over previous
.LBB0_1293:
	v_readlane_b32 s18, v252, 1
	v_readlane_b32 s19, v252, 2
	s_waitcnt lgkmcnt(0)
	s_barrier
	v_mbcnt_lo_u32_b32 v0, -1, 0
	v_mbcnt_hi_u32_b32 v0, -1, v0
	v_readlane_b32 s2, v252, 6
	v_mbcnt_lo_u32_b32 v4, -1, 0
	v_mbcnt_hi_u32_b32 v4, -1, v4
	s_movk_i32 s37, 0xe00
	v_readlane_b32 s2, v253, 20
	s_and_b64 vcc, exec, s[84:85]
	s_nop 0
	v_add_u32_e32 v0, s2, v4
	v_and_b32_e32 v1, 0x1ff, v0
	s_nop 0
	v_readfirstlane_b32 s36, v1
	s_cbranch_vccnz .LBB0_1318
	s_add_u32 s6, s18, 0x7200000
	v_readlane_b32 s2, v254, 3
	s_addc_u32 s7, s19, 0
	v_readlane_b32 s3, v254, 4
	s_xor_b32 s2, s2, 8
	s_add_u32 s10, s18, 0x10c00000
	v_lshlrev_b32_e32 v1, 4, v1
	v_and_b32_e32 v2, 32, v4
	s_mul_hi_i32 s23, s2, 0x1c0000
	s_mul_i32 s22, s2, 0x1c0000
	v_readlane_b32 s2, v254, 1
	s_addc_u32 s11, s19, 0
	s_lshr_b32 s38, s36, 6
	v_and_b32_e32 v5, 64, v0
	v_bitop3_b32 v6, v1, v2, 48 bitop3:0x6c
	v_lshrrev_b32_e32 v0, 3, v0
	v_bfe_u32 v1, v4, 2, 4
	v_readlane_b32 s3, v254, 2
	s_lshr_b32 s39, s36, 8
	s_lshl_b32 s31, s38, 10
	v_and_or_b32 v0, v0, 48, v1
	s_mul_hi_i32 s3, s2, 0x1c0000
	s_mul_i32 s2, s2, 0x1c0000
	v_mul_u32_u24_e32 v7, 0x1c00, v0
	s_add_u32 s2, s6, s2
	v_or3_b32 v160, v5, v6, v7
	s_addc_u32 s3, s7, s3
	s_add_i32 s33, s31, 0
	v_lshl_add_u64 v[0:1], s[2:3], 0, v[160:161]
	s_add_i32 m0, s33, 0x10000
	s_mov_b64 s[34:35], 0x70000
	global_load_lds_dwordx4 v160, s[2:3]
	v_lshl_add_u64 v[2:3], v[0:1], 0, s[34:35]
	s_add_i32 m0, s33, 0x12000
	s_mov_b64 s[12:13], 0x150000
	global_load_lds_dwordx4 v[2:3], off
	v_lshl_add_u64 v[2:3], v[0:1], 0, s[4:5]
	s_add_i32 m0, s33, 0x14000
	s_mov_b64 s[42:43], 0x150080
	global_load_lds_dwordx4 v[2:3], off
	s_add_i32 m0, s33, 0x16000
	s_add_u32 s22, s10, s22
	v_lshl_add_u64 v[2:3], v[0:1], 0, s[12:13]
	s_addc_u32 s23, s11, s23
	global_load_lds_dwordx4 v[2:3], off
	v_lshl_add_u64 v[2:3], s[22:23], 0, v[160:161]
	s_mov_b32 m0, s33
	s_add_i32 s48, s33, 0x2000
	global_load_lds_dwordx4 v160, s[22:23]
	v_lshl_add_u64 v[8:9], v[2:3], 0, s[34:35]
	s_mov_b32 m0, s48
	s_add_i32 s49, s33, 0x4000
	global_load_lds_dwordx4 v[8:9], off
	v_lshl_add_u64 v[8:9], v[2:3], 0, s[4:5]
	s_mov_b32 m0, s49
	s_add_i32 s50, s33, 0x6000
	global_load_lds_dwordx4 v[8:9], off
	v_lshl_add_u64 v[8:9], v[2:3], 0, s[12:13]
	s_mov_b32 m0, s50
	s_cmp_eq_u32 s39, 1
	global_load_lds_dwordx4 v[8:9], off
	s_cselect_b64 s[34:35], -1, 0
	s_cmp_lg_u32 s39, 1
	s_mov_b64 s[4:5], 0x70080
	s_mov_b64 s[12:13], 0xe0080
	s_cbranch_scc1 .LBB0_1296
	s_barrier
.LBB0_1296:
	s_add_u32 s40, s18, 0x2400000
	s_addc_u32 s41, s19, 0
	v_lshl_add_u64 v[8:9], v[0:1], 0, s[56:57]
	s_add_i32 m0, s33, 0x18000
	s_waitcnt vmcnt(2)
	s_barrier
	global_load_lds_dwordx4 v[8:9], off
	v_lshl_add_u64 v[8:9], v[0:1], 0, s[4:5]
	s_add_i32 m0, s33, 0x1a000
	s_add_i32 s51, s33, 0x8000
	global_load_lds_dwordx4 v[8:9], off
	v_lshl_add_u64 v[8:9], v[2:3], 0, s[56:57]
	s_mov_b32 m0, s51
	s_add_i32 s54, s33, 0xa000
	global_load_lds_dwordx4 v[8:9], off
	v_lshl_add_u64 v[2:3], v[2:3], 0, s[4:5]
	s_mov_b32 m0, s54
	s_ashr_i32 s18, s37, 31
	global_load_lds_dwordx4 v[2:3], off
	v_lshl_add_u64 v[2:3], v[0:1], 0, s[12:13]
	s_add_i32 m0, s33, 0x1c000
	v_lshl_add_u64 v[0:1], v[0:1], 0, s[42:43]
	global_load_lds_dwordx4 v[2:3], off
	s_add_i32 m0, s33, 0x1e000
	s_lshr_b32 s18, s18, 26
	global_load_lds_dwordx4 v[0:1], off
	v_bfe_u32 v1, v4, 4, 2
	v_and_b32_e32 v0, 15, v4
	v_lshlrev_b32_e32 v2, 4, v1
	s_add_i32 s18, s37, s18
	v_lshl_or_b32 v152, s39, 6, v0
	v_lshl_or_b32 v0, v0, 6, v2
	v_lshlrev_b32_e32 v2, 2, v4
	s_ashr_i32 s55, s18, 6
	s_lshl_b32 s18, s39, 13
	v_and_b32_e32 v2, 32, v2
	v_bitop3_b32 v3, v0, s18, v2 bitop3:0xde
	s_lshl_b32 s18, s38, 5
	s_and_b32 s18, s18, 0x60
	s_lshl_b32 s19, s18, 7
	v_bitop3_b32 v153, v0, s19, v2 bitop3:0xde
	s_cmp_gt_i32 s37, 63
	v_lshl_or_b32 v154, v1, 2, s18
	v_readlane_b32 s18, v254, 1
	s_waitcnt vmcnt(6)
	s_cselect_b64 s[42:43], -1, 0
	s_add_i32 s58, s55, -2
	v_readlane_b32 s19, v254, 2
	s_cmpk_lt_u32 s36, 0x100
	s_mov_b32 s74, s18
	v_readlane_b32 s18, v254, 3
	s_cselect_b64 s[44:45], -1, 0
	v_add3_u32 v128, v7, v6, v5
	v_mov_b32_e32 v129, v161
	s_mov_b32 s96, 0
	v_add_u32_e32 v155, 0, v3
	s_mov_b32 s75, s18
	s_xor_b32 s75, s75, 8
	s_barrier
	v_readlane_b32 s19, v254, 4
	s_branch .LBB0_1299

.LBB0_1304:
	s_ashr_i32 s18, s36, 3
	s_add_i32 s18, s46, s18
	s_ashr_i32 s19, s18, 31
	s_lshr_b32 s19, s19, 27
	s_add_i32 s19, s18, s19
	s_ashr_i32 s36, s19, 5
	s_and_b32 s19, s19, 0xffe0
	s_sub_i32 s18, s18, s19
	s_bfe_i32 s19, s18, 0x80000
	s_bfe_u32 s19, s19, 0x3000c
	s_add_i32 s19, s18, s19
	s_bfe_i32 s37, s19, 0x80000
	s_and_b32 s19, s19, 0xf8
	s_sub_i32 s18, s18, s19
	s_lshl_b32 s36, s36, 3
	s_sext_i32_i16 s37, s37
	s_sext_i32_i8 s18, s18
	s_add_i32 s59, s36, s18
	s_xor_b32 s59, s59, 8
	s_ashr_i32 s63, s37, 3
